# v15 + nt on P0's adaLN w_ada loads and part-1 w_in loads (read-once streams)
# speedup vs baseline: 1.0444x; 1.0444x over previous
; __device__ __forceinline__ void p0_adaln(Frame& F) {
;     ...
; #pragma unroll 8
;     for (int it = 0; it < 64; ++it) {
;         const int k = 256 * F.wave + 4 * it + kq;
;         const f32x4 w = *(const f32x4*)(wp + (size_t)it * 4 * 12288);
;         const float s0 = sil[k], s1 = sil[2048 + k], s2 = sil[4096 + k];
; #pragma unroll
;         for (int e = 0; e < 4; ++e) { acc[0][e] += s0 * w[e]; acc[1][e] += s1 * w[e]; acc[2][e] += s2 * w[e]; }
;     }
; #pragma unroll
;     for (int r = 0; r < 3; ++r)
; #pragma unroll
;         for (int e = 0; e < 4; ++e) { float v = acc[r][e]; v += __shfl_xor(v, 16); v += __shfl_xor(v, 32); if (kq == 0) red[(F.wave * 3 + r) * 64 + 4 * cq + e] = v; }
;     __syncthreads();
.LBB0_14:
	v_add_co_u32_e32 v20, vcc, s5, v12
	global_load_dwordx4 v[16:19], v[12:13], off nt
	s_nop 0
	v_addc_co_u32_e32 v21, vcc, -1, v13, vcc
	v_add_co_u32_e32 v24, vcc, s6, v12
	v_add_u32_e32 v48, s3, v1
	s_nop 0
	v_addc_co_u32_e32 v25, vcc, -1, v13, vcc
	v_add_co_u32_e32 v28, vcc, s7, v12
	v_add_u32_e32 v49, 0x11c00, v48
	s_nop 0
	v_addc_co_u32_e32 v29, vcc, -1, v13, vcc
	v_add_co_u32_e32 v32, vcc, s42, v12
	v_add_u32_e32 v50, 0x13c00, v48
	s_nop 0
	v_addc_co_u32_e32 v33, vcc, -1, v13, vcc
	v_add_co_u32_e32 v36, vcc, s43, v12
	global_load_dwordx4 v[20:23], v[20:21], off nt
	s_nop 0
	global_load_dwordx4 v[24:27], v[24:25], off nt
	s_nop 0
	global_load_dwordx4 v[28:31], v[28:29], off nt
	s_nop 0
	global_load_dwordx4 v[32:35], v[32:33], off nt
	v_addc_co_u32_e32 v37, vcc, 0, v13, vcc
	v_add_co_u32_e32 v40, vcc, s44, v12
	global_load_dwordx4 v[36:39], v[36:37], off nt
	s_nop 0
	v_addc_co_u32_e32 v41, vcc, 0, v13, vcc
	v_add_co_u32_e32 v44, vcc, s45, v12
	global_load_dwordx4 v[40:43], v[40:41], off nt
	s_nop 0
	v_addc_co_u32_e32 v45, vcc, 0, v13, vcc
	global_load_dwordx4 v[44:47], v[44:45], off nt
	v_add_u32_e32 v51, 0x15c00, v48
	v_add_u32_e32 v53, 0x11c10, v48
	v_add_u32_e32 v55, 0x13c10, v48
	v_add_u32_e32 v57, 0x15c10, v48
	v_add_u32_e32 v59, 0x11c20, v48
	v_add_u32_e32 v61, 0x13c20, v48
	v_add_u32_e32 v63, 0x15c20, v48
	v_add_u32_e32 v65, 0x11c30, v48
	v_add_u32_e32 v67, 0x13c30, v48
	v_add_u32_e32 v69, 0x15c30, v48
	v_add_u32_e32 v71, 0x11c40, v48
	v_add_u32_e32 v73, 0x13c40, v48
	v_add_u32_e32 v75, 0x15c40, v48
	v_add_u32_e32 v77, 0x11c50, v48
	v_add_u32_e32 v79, 0x13c50, v48
	v_add_u32_e32 v81, 0x15c50, v48
	v_add_u32_e32 v83, 0x11c60, v48
	v_add_u32_e32 v85, 0x13c60, v48
	v_add_u32_e32 v87, 0x15c60, v48
	v_add_u32_e32 v89, 0x11c70, v48
	v_add_u32_e32 v91, 0x13c70, v48
	v_add_u32_e32 v93, 0x15c70, v48
	ds_read_b32 v48, v49
	ds_read_b32 v50, v50
	ds_read_b32 v52, v51
	ds_read_b32 v54, v53
	ds_read_b32 v56, v55
	ds_read_b32 v58, v57
	ds_read_b32 v60, v59
	ds_read_b32 v62, v61
	ds_read_b32 v64, v63
	ds_read_b32 v66, v65
	ds_read_b32 v68, v67
	ds_read_b32 v70, v69
	ds_read_b32 v72, v71
	ds_read_b32 v74, v73
	ds_read_b32 v76, v75
	ds_read_b32 v78, v77
	ds_read_b32 v80, v79
	ds_read_b32 v82, v81
	ds_read_b32 v84, v83
	ds_read_b32 v86, v85
	ds_read_b32 v88, v87
	ds_read_b32 v90, v89
	ds_read_b32 v92, v91
	ds_read_b32 v94, v93
	s_addk_i32 s3, 0x80
	v_lshl_add_u64 v[12:13], v[12:13], 0, s[38:39]
	s_cmp_eq_u32 s3, 0
	s_waitcnt vmcnt(6) lgkmcnt(14)
	v_pk_fma_f32 v[14:15], v[48:49], v[20:21], v[14:15] op_sel_hi:[0,1,1]
	v_pk_fma_f32 v[10:11], v[48:49], v[22:23], v[10:11] op_sel_hi:[0,1,1]
	v_pk_fma_f32 v[8:9], v[20:21], v[50:51], v[8:9] op_sel_hi:[1,0,1]
	v_pk_fma_f32 v[6:7], v[22:23], v[50:51], v[6:7] op_sel_hi:[1,0,1]
	v_pk_fma_f32 v[4:5], v[20:21], v[52:53], v[4:5] op_sel_hi:[1,0,1]
	v_pk_fma_f32 v[2:3], v[22:23], v[52:53], v[2:3] op_sel_hi:[1,0,1]
	s_waitcnt vmcnt(5)
	v_pk_fma_f32 v[14:15], v[54:55], v[24:25], v[14:15] op_sel_hi:[0,1,1]
	v_pk_fma_f32 v[10:11], v[54:55], v[26:27], v[10:11] op_sel_hi:[0,1,1]
	v_pk_fma_f32 v[8:9], v[24:25], v[56:57], v[8:9] op_sel_hi:[1,0,1]
	v_pk_fma_f32 v[6:7], v[26:27], v[56:57], v[6:7] op_sel_hi:[1,0,1]
	v_pk_fma_f32 v[4:5], v[24:25], v[58:59], v[4:5] op_sel_hi:[1,0,1]
	v_pk_fma_f32 v[2:3], v[26:27], v[58:59], v[2:3] op_sel_hi:[1,0,1]
	s_waitcnt vmcnt(4)
	v_pk_fma_f32 v[14:15], v[60:61], v[28:29], v[14:15] op_sel_hi:[0,1,1]
	v_pk_fma_f32 v[10:11], v[60:61], v[30:31], v[10:11] op_sel_hi:[0,1,1]
	v_pk_fma_f32 v[8:9], v[28:29], v[62:63], v[8:9] op_sel_hi:[1,0,1]
	v_pk_fma_f32 v[6:7], v[30:31], v[62:63], v[6:7] op_sel_hi:[1,0,1]
	v_pk_fma_f32 v[4:5], v[28:29], v[64:65], v[4:5] op_sel_hi:[1,0,1]
	v_pk_fma_f32 v[2:3], v[30:31], v[64:65], v[2:3] op_sel_hi:[1,0,1]
	s_waitcnt vmcnt(3)
	v_pk_fma_f32 v[14:15], v[66:67], v[32:33], v[14:15] op_sel_hi:[0,1,1]
	v_pk_fma_f32 v[10:11], v[66:67], v[34:35], v[10:11] op_sel_hi:[0,1,1]
	s_waitcnt lgkmcnt(13)
	v_pk_fma_f32 v[8:9], v[32:33], v[68:69], v[8:9] op_sel_hi:[1,0,1]
	v_pk_fma_f32 v[6:7], v[34:35], v[68:69], v[6:7] op_sel_hi:[1,0,1]
	s_waitcnt lgkmcnt(12)
	v_pk_fma_f32 v[4:5], v[32:33], v[70:71], v[4:5] op_sel_hi:[1,0,1]
	v_pk_fma_f32 v[2:3], v[34:35], v[70:71], v[2:3] op_sel_hi:[1,0,1]
	s_waitcnt lgkmcnt(11)
	v_pk_fma_f32 v[14:15], v[72:73], v[16:17], v[14:15] op_sel_hi:[0,1,1]
	s_waitcnt lgkmcnt(10)
	v_pk_fma_f32 v[8:9], v[16:17], v[74:75], v[8:9] op_sel_hi:[1,0,1]
	s_waitcnt lgkmcnt(9)
	v_pk_fma_f32 v[4:5], v[16:17], v[76:77], v[4:5] op_sel_hi:[1,0,1]
	v_pk_fma_f32 v[10:11], v[72:73], v[18:19], v[10:11] op_sel_hi:[0,1,1]
	v_pk_fma_f32 v[6:7], v[18:19], v[74:75], v[6:7] op_sel_hi:[1,0,1]
	v_pk_fma_f32 v[2:3], v[18:19], v[76:77], v[2:3] op_sel_hi:[1,0,1]
	s_waitcnt vmcnt(2) lgkmcnt(8)
	v_pk_fma_f32 v[14:15], v[78:79], v[36:37], v[14:15] op_sel_hi:[0,1,1]
	s_waitcnt lgkmcnt(7)
	v_pk_fma_f32 v[8:9], v[36:37], v[80:81], v[8:9] op_sel_hi:[1,0,1]
	s_waitcnt lgkmcnt(6)
	v_pk_fma_f32 v[4:5], v[36:37], v[82:83], v[4:5] op_sel_hi:[1,0,1]
	v_pk_fma_f32 v[10:11], v[78:79], v[38:39], v[10:11] op_sel_hi:[0,1,1]
	v_pk_fma_f32 v[6:7], v[38:39], v[80:81], v[6:7] op_sel_hi:[1,0,1]
	v_pk_fma_f32 v[2:3], v[38:39], v[82:83], v[2:3] op_sel_hi:[1,0,1]
	s_waitcnt vmcnt(1) lgkmcnt(5)
	v_pk_fma_f32 v[14:15], v[84:85], v[40:41], v[14:15] op_sel_hi:[0,1,1]
	s_waitcnt lgkmcnt(4)
	v_pk_fma_f32 v[8:9], v[40:41], v[86:87], v[8:9] op_sel_hi:[1,0,1]
	s_waitcnt lgkmcnt(3)
	v_pk_fma_f32 v[4:5], v[40:41], v[88:89], v[4:5] op_sel_hi:[1,0,1]
	v_pk_fma_f32 v[10:11], v[84:85], v[42:43], v[10:11] op_sel_hi:[0,1,1]
	v_pk_fma_f32 v[6:7], v[42:43], v[86:87], v[6:7] op_sel_hi:[1,0,1]
	v_pk_fma_f32 v[2:3], v[42:43], v[88:89], v[2:3] op_sel_hi:[1,0,1]
	s_waitcnt vmcnt(0) lgkmcnt(2)
	v_pk_fma_f32 v[14:15], v[90:91], v[44:45], v[14:15] op_sel_hi:[0,1,1]
	s_waitcnt lgkmcnt(1)
	v_pk_fma_f32 v[8:9], v[44:45], v[92:93], v[8:9] op_sel_hi:[1,0,1]
	s_waitcnt lgkmcnt(0)
	v_pk_fma_f32 v[4:5], v[44:45], v[94:95], v[4:5] op_sel_hi:[1,0,1]
	v_pk_fma_f32 v[10:11], v[90:91], v[46:47], v[10:11] op_sel_hi:[0,1,1]
	v_pk_fma_f32 v[6:7], v[46:47], v[92:93], v[6:7] op_sel_hi:[1,0,1]
	v_pk_fma_f32 v[2:3], v[46:47], v[94:95], v[2:3] op_sel_hi:[1,0,1]
	s_cbranch_scc0 .LBB0_14
	v_mbcnt_lo_u32_b32 v1, -1, 0
	v_mbcnt_hi_u32_b32 v1, -1, v1
	v_and_b32_e32 v13, 64, v1
	v_xor_b32_e32 v12, 16, v1
	v_add_u32_e32 v13, 64, v13
	v_cmp_lt_i32_e32 vcc, v12, v13
	v_xor_b32_e32 v16, 32, v1
	s_add_i32 s3, 0, 0x17800
	v_cndmask_b32_e32 v12, v1, v12, vcc
	v_lshlrev_b32_e32 v12, 2, v12
	ds_bpermute_b32 v17, v12, v14
	v_cmp_lt_i32_e32 vcc, v16, v13
	s_nop 1
	v_cndmask_b32_e32 v1, v1, v16, vcc
	v_lshlrev_b32_e32 v13, 2, v1
	s_waitcnt lgkmcnt(0)
	v_add_f32_e32 v16, v14, v17
	ds_bpermute_b32 v17, v13, v16
	v_lshl_add_u32 v1, v170, 4, s3
	v_readlane_b32 s3, v255, 8
	s_mulk_i32 s3, 0x300
	v_cmp_gt_u32_e32 vcc, 16, v170
	v_add_u32_e32 v14, s3, v1
	s_and_saveexec_b64 s[38:39], vcc
	s_cbranch_execz .LBB0_17
	s_waitcnt lgkmcnt(0)
	v_add_f32_e32 v16, v16, v17
	ds_write_b32 v14, v16

; #define LAS __attribute__((address_space(3)))
; #define LDS_WAIT() asm volatile("s_waitcnt lgkmcnt(0)" ::: "memory")
; __device__ __forceinline__ void p0_transpose_item(const float* W, int N, int k0, int n0, bf16_t* dst, int dK, bool rope_perm, LAS float* scr, int lane) {
; #pragma unroll 8
;     for (int i = 0; i < 32; ++i) { const int kk = 2 * i + (lane >> 5); scr[kk * 33 + (lane & 31)] = W[(size_t)(k0 + kk) * N + n0 + (lane & 31)]; }
;     LDS_WAIT(); asm volatile("" ::: "memory");
.LBB0_47:
	s_lshl_b32 s73, s69, 1
	s_lshl_b32 s74, s70, 1
	v_or_b32_e32 v27, s73, v1
	v_or_b32_e32 v60, s74, v4
	s_add_i32 s75, s73, 4
	s_add_i32 s76, s74, 4
	s_add_i32 s77, s73, 8
	s_add_i32 s78, s74, 8
	s_add_i32 s79, s73, 12
	s_add_i32 s84, s74, 12
	s_add_i32 s85, s73, 16
	s_add_i32 s86, s74, 16
	s_add_i32 s87, s73, 20
	s_add_i32 s88, s74, 20
	s_add_i32 s89, s73, 24
	s_add_i32 s90, s74, 24
	s_add_i32 s73, s73, 28
	s_add_i32 s74, s74, 28
	v_add_u32_e32 v28, s4, v60
	v_or_b32_e32 v61, s75, v1
	v_or_b32_e32 v62, s76, v4
	v_or_b32_e32 v63, s77, v1
	v_or_b32_e32 v64, s78, v4
	v_or_b32_e32 v65, s79, v1
	v_or_b32_e32 v66, s84, v4
	v_or_b32_e32 v67, s85, v1
	v_or_b32_e32 v68, s86, v4
	v_or_b32_e32 v69, s87, v1
	v_or_b32_e32 v70, s88, v4
	v_or_b32_e32 v71, s89, v1
	v_or_b32_e32 v72, s90, v4
	v_or_b32_e32 v73, s73, v1
	v_or_b32_e32 v74, s74, v4
	v_add_u32_e32 v30, s68, v27
	v_mad_i64_i32 v[28:29], s[74:75], v28, s43, v[20:21]
	v_add_u32_e32 v34, s68, v61
	v_add_u32_e32 v32, s4, v62
	v_add_u32_e32 v38, s68, v63
	v_add_u32_e32 v36, s4, v64
	v_add_u32_e32 v42, s68, v65
	v_add_u32_e32 v40, s4, v66
	v_add_u32_e32 v46, s68, v67
	v_add_u32_e32 v44, s4, v68
	v_add_u32_e32 v50, s68, v69
	v_add_u32_e32 v48, s4, v70
	v_add_u32_e32 v54, s68, v71
	v_add_u32_e32 v52, s4, v72
	v_add_u32_e32 v58, s68, v73
	v_add_u32_e32 v56, s4, v74
	v_mad_i64_i32 v[30:31], s[74:75], v30, s43, v[20:21]
	v_mad_i64_i32 v[32:33], s[74:75], v32, s43, v[20:21]
	v_mad_i64_i32 v[34:35], s[74:75], v34, s43, v[20:21]
	v_mad_i64_i32 v[36:37], s[74:75], v36, s43, v[20:21]
	v_mad_i64_i32 v[38:39], s[74:75], v38, s43, v[20:21]
	v_mad_i64_i32 v[40:41], s[74:75], v40, s43, v[20:21]
	v_mad_i64_i32 v[42:43], s[74:75], v42, s43, v[20:21]
	v_mad_i64_i32 v[44:45], s[74:75], v44, s43, v[20:21]
	v_mad_i64_i32 v[46:47], s[74:75], v46, s43, v[20:21]
	v_mad_i64_i32 v[48:49], s[74:75], v48, s43, v[20:21]
	v_mad_i64_i32 v[50:51], s[74:75], v50, s43, v[20:21]
	v_mad_i64_i32 v[52:53], s[74:75], v52, s43, v[20:21]
	v_mad_i64_i32 v[54:55], s[74:75], v54, s43, v[20:21]
	v_mad_i64_i32 v[56:57], s[74:75], v56, s43, v[20:21]
	v_mad_i64_i32 v[58:59], s[74:75], v58, s43, v[20:21]
	global_load_dword v75, v[28:29], off nt
	global_load_dword v76, v[30:31], off nt
	global_load_dword v77, v[32:33], off nt
	global_load_dword v78, v[34:35], off nt
	global_load_dword v79, v[36:37], off nt
	global_load_dword v80, v[38:39], off nt
	global_load_dword v81, v[40:41], off nt
	global_load_dword v82, v[42:43], off nt
	global_load_dword v83, v[44:45], off nt
	global_load_dword v84, v[46:47], off nt
	global_load_dword v85, v[48:49], off nt
	global_load_dword v86, v[50:51], off nt
	global_load_dword v87, v[52:53], off nt
	global_load_dword v88, v[54:55], off nt
	global_load_dword v89, v[56:57], off nt
	global_load_dword v90, v[58:59], off nt
	s_add_i32 s70, s70, 16
	s_add_i32 s69, s69, 16
	s_add_i32 s71, s71, -16
	v_mad_u64_u32 v[28:29], s[74:75], v60, s42, v[10:11]
	s_cmp_lg_u32 s71, 0
	v_mad_u64_u32 v[30:31], s[74:75], v27, s42, v[10:11]
	v_mad_u64_u32 v[32:33], s[74:75], v62, s42, v[10:11]
	v_mad_u64_u32 v[34:35], s[74:75], v61, s42, v[10:11]
	v_mad_u64_u32 v[36:37], s[74:75], v64, s42, v[10:11]
	v_mad_u64_u32 v[38:39], s[74:75], v63, s42, v[10:11]
	v_mad_u64_u32 v[40:41], s[74:75], v66, s42, v[10:11]
	v_mad_u64_u32 v[42:43], s[74:75], v65, s42, v[10:11]
	v_mad_u64_u32 v[44:45], s[74:75], v68, s42, v[10:11]
	v_mad_u64_u32 v[46:47], s[74:75], v67, s42, v[10:11]
	v_mad_u64_u32 v[48:49], s[74:75], v70, s42, v[10:11]
	v_mad_u64_u32 v[50:51], s[74:75], v69, s42, v[10:11]
	v_mad_u64_u32 v[52:53], s[74:75], v72, s42, v[10:11]
	v_mad_u64_u32 v[54:55], s[74:75], v71, s42, v[10:11]
	v_mad_u64_u32 v[56:57], s[74:75], v74, s42, v[10:11]
	v_mad_u64_u32 v[58:59], s[74:75], v73, s42, v[10:11]
	s_waitcnt vmcnt(15)
	ds_write_b32 v28, v75
	s_waitcnt vmcnt(14)
	ds_write_b32 v30, v76
	s_waitcnt vmcnt(13)
	ds_write_b32 v32, v77
	s_waitcnt vmcnt(12)
	ds_write_b32 v34, v78
	s_waitcnt vmcnt(11)
	ds_write_b32 v36, v79
	s_waitcnt vmcnt(10)
	ds_write_b32 v38, v80
	s_waitcnt vmcnt(9)
	ds_write_b32 v40, v81
	s_waitcnt vmcnt(8)
	ds_write_b32 v42, v82
	s_waitcnt vmcnt(7)
	ds_write_b32 v44, v83
	s_waitcnt vmcnt(6)
	ds_write_b32 v46, v84
	s_waitcnt vmcnt(5)
	ds_write_b32 v48, v85
	s_waitcnt vmcnt(4)
	ds_write_b32 v50, v86
	s_waitcnt vmcnt(3)
	ds_write_b32 v52, v87
	s_waitcnt vmcnt(2)
	ds_write_b32 v54, v88
	s_waitcnt vmcnt(1)
	ds_write_b32 v56, v89
	s_waitcnt vmcnt(0)
	ds_write_b32 v58, v90
	s_cbranch_scc1 .LBB0_47
; #define LAS __attribute__((address_space(3)))
; #define LDS_WAIT() asm volatile("s_waitcnt lgkmcnt(0)" ::: "memory")
; __device__ __forceinline__ unsigned f2bf(float f) { unsigned u = __float_as_uint(f); return (u + 0x7fffu + ((u >> 16) & 1u)) >> 16; }
; __device__ __forceinline__ unsigned pk2(float lo, float hi) { return f2bf(lo) | (f2bf(hi) << 16); }
; __device__ __forceinline__ void p0_transpose_item(const float* W, int N, int k0, int n0, bf16_t* dst, int dK, bool rope_perm, LAS float* scr, int lane) {
; #pragma unroll 8
;     for (int i = 0; i < 32; ++i) { const int kk = 2 * i + (lane >> 5); scr[kk * 33 + (lane & 31)] = W[(size_t)(k0 + kk) * N + n0 + (lane & 31)]; }
;     LDS_WAIT(); asm volatile("" ::: "memory");
;     const int c = lane & 7;
; #pragma unroll
;     for (int j = 0; j < 4; ++j) { const int n = (lane >> 3) + 8 * j; const int ns = rope_perm ? (16 * ((n >> 2) & 1) + 4 * (n >> 3) + (n & 3)) : n; const LAS float* s = scr + (8 * c) * 33 + ns;
;         u32x4 o; o.x = pk2(s[0 * 33], s[1 * 33]); o.y = pk2(s[2 * 33], s[3 * 33]); o.z = pk2(s[4 * 33], s[5 * 33]); o.w = pk2(s[6 * 33], s[7 * 33]);
;         *(u32x4*)(dst + (size_t)n * dK + k0 + 8 * c) = o; }
;     LDS_WAIT(); asm volatile("" ::: "memory");
	s_lshl_b64 s[38:39], s[38:39], 12
	s_add_u32 s70, s6, s38
	s_addc_u32 s71, s7, s39
	s_cmp_eq_u32 s5, 5
	s_cselect_b64 s[38:39], -1, 0
	s_cmp_eq_u32 s5, 2
	s_cselect_b64 s[68:69], -1, 0
	s_or_b64 vcc, s[68:69], s[38:39]
	s_waitcnt lgkmcnt(0)
	v_cndmask_b32_e32 v20, v2, v3, vcc
	v_lshl_add_u32 v27, v20, 2, v5
	ds_read2_b32 v[20:21], v27 offset1:33
	ds_read2_b32 v[30:31], v27 offset0:66 offset1:99
	ds_read2_b32 v[34:35], v27 offset0:198 offset1:231
	s_ashr_i32 s5, s4, 31
	s_lshl_b64 s[4:5], s[4:5], 1
	s_waitcnt lgkmcnt(2)
	v_bfe_u32 v28, v20, 16, 1
	v_add3_u32 v20, v20, v28, s44
	v_bfe_u32 v28, v21, 16, 1
	v_lshrrev_b32_e32 v20, 16, v20
	v_add3_u32 v21, v21, v28, s44
	v_and_or_b32 v28, v21, s45, v20
	s_waitcnt lgkmcnt(1)
	v_bfe_u32 v20, v30, 16, 1
	v_add3_u32 v29, v30, v20, s44
	ds_read2_b32 v[20:21], v27 offset0:132 offset1:165
	v_bfe_u32 v30, v31, 16, 1
	v_lshrrev_b32_e32 v29, 16, v29
	v_add3_u32 v30, v31, v30, s44
	v_and_or_b32 v29, v30, s45, v29
	s_waitcnt lgkmcnt(0)
	v_bfe_u32 v30, v20, 16, 1
	v_add3_u32 v20, v20, v30, s44
	v_bfe_u32 v27, v21, 16, 1
	v_lshrrev_b32_e32 v20, 16, v20
	v_add3_u32 v21, v21, v27, s44
	v_and_or_b32 v30, v21, s45, v20
	v_bfe_u32 v20, v34, 16, 1
	v_add3_u32 v20, v34, v20, s44
	v_lshrrev_b32_e32 v27, 16, v20
	v_cndmask_b32_e32 v20, v11, v22, vcc
	s_add_u32 s4, s70, s4
	v_lshl_add_u32 v36, v20, 2, v5
	s_addc_u32 s5, s71, s5
	v_bfe_u32 v31, v35, 16, 1
	ds_read2_b32 v[20:21], v36 offset1:33
	v_lshl_add_u64 v[32:33], s[4:5], 0, v[6:7]
	v_add3_u32 v31, v35, v31, s44
	v_and_or_b32 v31, v31, s45, v27
	v_lshl_add_u64 v[34:35], v[32:33], 0, v[12:13]
	global_store_dwordx4 v[34:35], v[28:31], off sc0 sc1
	ds_read2_b32 v[30:31], v36 offset0:66 offset1:99
	s_waitcnt lgkmcnt(1)
	v_bfe_u32 v27, v20, 16, 1
	v_add3_u32 v20, v20, v27, s44
	v_bfe_u32 v27, v21, 16, 1
	v_lshrrev_b32_e32 v20, 16, v20
	v_add3_u32 v21, v21, v27, s44
	v_and_or_b32 v28, v21, s45, v20
	s_waitcnt lgkmcnt(0)
	v_bfe_u32 v20, v30, 16, 1
	v_add3_u32 v27, v30, v20, s44
	ds_read2_b32 v[20:21], v36 offset0:132 offset1:165
	v_bfe_u32 v29, v31, 16, 1
	ds_read2_b32 v[34:35], v36 offset0:198 offset1:231
	v_lshrrev_b32_e32 v27, 16, v27
	v_add3_u32 v29, v31, v29, s44
	v_and_or_b32 v29, v29, s45, v27
	s_waitcnt lgkmcnt(1)
	v_bfe_u32 v27, v20, 16, 1
	v_add3_u32 v20, v20, v27, s44
	v_bfe_u32 v27, v21, 16, 1
	v_lshrrev_b32_e32 v20, 16, v20
	v_add3_u32 v21, v21, v27, s44
	v_and_or_b32 v30, v21, s45, v20
	s_waitcnt lgkmcnt(0)
	v_bfe_u32 v20, v34, 16, 1
	v_add3_u32 v20, v34, v20, s44
	v_lshrrev_b32_e32 v27, 16, v20
	v_cndmask_b32_e32 v20, v23, v24, vcc
	v_lshl_add_u32 v36, v20, 2, v5
	v_bfe_u32 v31, v35, 16, 1
	ds_read2_b32 v[20:21], v36 offset1:33
	v_add3_u32 v31, v35, v31, s44
	v_and_or_b32 v31, v31, s45, v27
	v_lshl_add_u64 v[34:35], v[32:33], 0, v[14:15]
	global_store_dwordx4 v[34:35], v[28:31], off sc0 sc1
	ds_read2_b32 v[30:31], v36 offset0:66 offset1:99
	s_waitcnt lgkmcnt(1)
	v_bfe_u32 v27, v20, 16, 1
	v_add3_u32 v20, v20, v27, s44
	v_bfe_u32 v27, v21, 16, 1
	v_lshrrev_b32_e32 v20, 16, v20
	v_add3_u32 v21, v21, v27, s44
	v_and_or_b32 v28, v21, s45, v20
	s_waitcnt lgkmcnt(0)
	v_bfe_u32 v20, v30, 16, 1
	v_add3_u32 v27, v30, v20, s44
	ds_read2_b32 v[20:21], v36 offset0:132 offset1:165
	v_bfe_u32 v29, v31, 16, 1
	ds_read2_b32 v[34:35], v36 offset0:198 offset1:231
	v_lshrrev_b32_e32 v27, 16, v27
	v_add3_u32 v29, v31, v29, s44
	v_and_or_b32 v29, v29, s45, v27
	s_waitcnt lgkmcnt(1)
	v_bfe_u32 v27, v20, 16, 1
	v_add3_u32 v20, v20, v27, s44
	v_bfe_u32 v27, v21, 16, 1
	v_lshrrev_b32_e32 v20, 16, v20
	v_add3_u32 v21, v21, v27, s44
	v_and_or_b32 v30, v21, s45, v20
	s_waitcnt lgkmcnt(0)
	v_bfe_u32 v20, v34, 16, 1
	v_add3_u32 v20, v34, v20, s44
	v_lshrrev_b32_e32 v27, 16, v20
	v_cndmask_b32_e32 v20, v25, v26, vcc
	v_lshl_add_u32 v36, v20, 2, v5
	v_bfe_u32 v31, v35, 16, 1
	ds_read2_b32 v[20:21], v36 offset1:33
	v_add3_u32 v31, v35, v31, s44
	v_and_or_b32 v31, v31, s45, v27
	v_lshl_add_u64 v[34:35], v[32:33], 0, v[16:17]
	global_store_dwordx4 v[34:35], v[28:31], off sc0 sc1
	ds_read2_b32 v[30:31], v36 offset0:66 offset1:99
	s_waitcnt lgkmcnt(1)
	v_bfe_u32 v27, v20, 16, 1
	v_add3_u32 v20, v20, v27, s44
	v_bfe_u32 v27, v21, 16, 1
	v_lshrrev_b32_e32 v20, 16, v20
	v_add3_u32 v21, v21, v27, s44
	v_and_or_b32 v28, v21, s45, v20
	s_waitcnt lgkmcnt(0)
	v_bfe_u32 v20, v30, 16, 1
	v_add3_u32 v27, v30, v20, s44
	ds_read2_b32 v[20:21], v36 offset0:132 offset1:165
	v_bfe_u32 v29, v31, 16, 1
	ds_read2_b32 v[34:35], v36 offset0:198 offset1:231
	v_lshrrev_b32_e32 v27, 16, v27
	v_add3_u32 v29, v31, v29, s44
	v_and_or_b32 v29, v29, s45, v27
	s_waitcnt lgkmcnt(1)
	v_bfe_u32 v27, v20, 16, 1
	v_add3_u32 v20, v20, v27, s44
	v_bfe_u32 v27, v21, 16, 1
	v_lshrrev_b32_e32 v20, 16, v20
	v_add3_u32 v21, v21, v27, s44
	v_and_or_b32 v30, v21, s45, v20
	s_waitcnt lgkmcnt(0)
	v_bfe_u32 v20, v34, 16, 1
	v_add3_u32 v20, v34, v20, s44
	v_bfe_u32 v21, v35, 16, 1
	v_lshrrev_b32_e32 v20, 16, v20
	v_add3_u32 v21, v35, v21, s44
	v_and_or_b32 v31, v21, s45, v20
	v_lshl_add_u64 v[20:21], v[32:33], 0, v[18:19]
	global_store_dwordx4 v[20:21], v[28:31], off sc0 sc1
	s_waitcnt lgkmcnt(0)
	s_branch .LBB0_44
